# mixer GEMM epilogue rewritten: g1 loaded once per unit, residual loads in a 6/12-deep ring with counted vmcnt (was 16 load-wait-store round trips)
# baseline (speedup 1.0000x reference)
; __device__ __forceinline__ unsigned pk2(float lo, float hi) { return f2bf(lo) | (f2bf(hi) << 16); }
;     __device__ __forceinline__ void epi(const f32x4 (&acc)[2][2][4][2], const Unit& u, int wr, int wc, int fr, int fq) const {
;         const int rowt = (u.pm + pm0) * 256; const int mb = rowt < NL ? (rowt >> 12) : 4;
;         const bool f32in = xl != nullptr;
;         const char* xin = f32in ? (const char*)(rowt < NL ? xl + (size_t)rowt * DM : xc + (size_t)(rowt - NL) * DM) + (size_t)u.pn * 1024 : (const char*)(x1 + (size_t)rowt * DM) + (size_t)u.pn * 512;
;         const char* g1 = (const char*)(modv + mb * NMODW + 2 * DM) + (size_t)u.pn * 1024;
;         char* xo = (char*)(XM + (size_t)rowt * DM) + (size_t)u.pn * 512;
;         unsigned lcol = (unsigned)(wc * 32 + 8 * fq), lrow = (unsigned)(wr * 64 + fr); asm volatile("" : "+v"(lcol), "+v"(lrow));
;         const unsigned loff4 = (lrow * DM + lcol) * 4u, loff2 = (lrow * DM + lcol) * 2u;
; #pragma unroll
;         for (int ai = 0; ai < 2; ++ai)
; #pragma unroll
;             for (int m = 0; m < 4; ++m) { const size_t ro = (size_t)(ai * 128 + m * 16) * DM;
; #pragma unroll
;                 for (int bj = 0; bj < 2; ++bj) { const int cofs = bj * 128;
;                     const f32x4 g0 = *(const f32x4*)(g1 + cofs * 4 + lcol * 4), g1v = *(const f32x4*)(g1 + cofs * 4 + lcol * 4 + 16);
;                     f32x4 x0, x1v;
;                     if (f32in) { x0 = *(const f32x4*)(xin + (ro + cofs) * 4 + loff4); x1v = *(const f32x4*)(xin + (ro + cofs) * 4 + loff4 + 16); }
;                     else { const u32x4 w = *(const u32x4*)(xin + (ro + cofs) * 2 + loff2); x0 = (f32x4){bflo(w.x), bfhi(w.x), bflo(w.y), bfhi(w.y)}; x1v = (f32x4){bflo(w.z), bfhi(w.z), bflo(w.w), bfhi(w.w)}; }
;                     const f32x4 o0 = x0 + g0 * acc[ai][bj][m][0], o1 = x1v + g1v * acc[ai][bj][m][1];
;                     u32x4 ow; ow.x = pk2(o0[0], o0[1]); ow.y = pk2(o0[2], o0[3]); ow.z = pk2(o1[0], o1[1]); ow.w = pk2(o1[2], o1[3]);
;                     *(u32x4*)(xo + (ro + cofs) * 2 + loff2) = ow; }
;                 asm volatile("" ::: "memory"); }
.LBB0_1769:
	s_min_i32 s12, s24, 64
	s_lshr_b32 s12, s12, 4
	s_mul_i32 s12, s12, 0xc000
	s_lshl_b32 s17, s26, 10
	s_add_i32 s12, s12, s17
	s_add_i32 s12, s12, 0x104000
	s_add_u32 s46, s71, s12
	s_addc_u32 s47, s72, 0
	v_lshlrev_b32_e32 v146, 2, v170
	global_load_dwordx4 v[130:133], v146, s[46:47]
	global_load_dwordx4 v[134:137], v146, s[46:47] offset:16
	global_load_dwordx4 v[138:141], v146, s[46:47] offset:512
	global_load_dwordx4 v[142:145], v146, s[46:47] offset:528
	v_lshl_add_u32 v160, v168, 11, v170
	v_lshlrev_b32_e32 v160, 1, v160
	s_lshl_b32 s12, s24, 20
	s_lshl_b32 s17, s26, 9
	s_add_i32 s12, s12, s17
	s_add_u32 s44, s69, s12
	s_addc_u32 s45, s70, 0
	s_and_b64 vcc, exec, s[8:9]
	s_cbranch_vccz .Lmx_bf16
	v_lshlrev_b32_e32 v161, 1, v160
	s_cmp_gt_i32 s24, 63
	s_cbranch_scc1 .Lmx_ctx
	s_lshl_b32 s12, s24, 21
	s_add_u32 s42, s6, s12
	s_addc_u32 s43, s7, 0
	s_branch .Lmx_f32go
.Lmx_ctx:
	s_add_i32 s12, s24, -64
	s_lshl_b32 s12, s12, 21
	s_add_u32 s42, s66, s12
	s_addc_u32 s43, s65, 0
.Lmx_f32go:
	s_lshl_b32 s17, s26, 10
	s_add_u32 s42, s42, s17
	s_addc_u32 s43, s43, 0
	global_load_dwordx4 v[172:175], v161, s[42:43] offset:0
	global_load_dwordx4 v[176:179], v161, s[42:43] offset:16
	global_load_dwordx4 v[182:185], v161, s[42:43] offset:512
	global_load_dwordx4 v[186:189], v161, s[42:43] offset:528
	s_add_u32 s42, s42, 0x20000
	s_addc_u32 s43, s43, 0
	global_load_dwordx4 v[190:193], v161, s[42:43] offset:0
	global_load_dwordx4 v[194:197], v161, s[42:43] offset:16
	global_load_dwordx4 v[198:201], v161, s[42:43] offset:512
	global_load_dwordx4 v[202:205], v161, s[42:43] offset:528
	s_add_u32 s42, s42, 0x20000
	s_addc_u32 s43, s43, 0
	global_load_dwordx4 v[206:209], v161, s[42:43] offset:0
	global_load_dwordx4 v[216:219], v161, s[42:43] offset:16
	global_load_dwordx4 v[226:229], v161, s[42:43] offset:512
	global_load_dwordx4 v[230:233], v161, s[42:43] offset:528
	s_waitcnt vmcnt(10)
	v_pk_fma_f32 v[126:127], v[126:127], v[130:131], v[172:173]
	v_pk_fma_f32 v[128:129], v[128:129], v[132:133], v[174:175]
	v_pk_fma_f32 v[122:123], v[122:123], v[134:135], v[176:177]
	v_pk_fma_f32 v[124:125], v[124:125], v[136:137], v[178:179]
	s_add_u32 s42, s42, 0x20000
	s_addc_u32 s43, s43, 0
	global_load_dwordx4 v[172:175], v161, s[42:43] offset:0
	global_load_dwordx4 v[176:179], v161, s[42:43] offset:16
	v_cvt_pk_bf16_f32 v126, v126, v127
	v_cvt_pk_bf16_f32 v127, v128, v129
	v_cvt_pk_bf16_f32 v128, v122, v123
	v_cvt_pk_bf16_f32 v129, v124, v125
	global_store_dwordx4 v160, v[126:129], s[44:45] offset:0
	s_waitcnt vmcnt(11)
	v_pk_fma_f32 v[118:119], v[118:119], v[138:139], v[182:183]
	v_pk_fma_f32 v[120:121], v[120:121], v[140:141], v[184:185]
	v_pk_fma_f32 v[114:115], v[114:115], v[142:143], v[186:187]
	v_pk_fma_f32 v[116:117], v[116:117], v[144:145], v[188:189]
	global_load_dwordx4 v[182:185], v161, s[42:43] offset:512
	global_load_dwordx4 v[186:189], v161, s[42:43] offset:528
	v_cvt_pk_bf16_f32 v118, v118, v119
	v_cvt_pk_bf16_f32 v119, v120, v121
	v_cvt_pk_bf16_f32 v120, v114, v115
	v_cvt_pk_bf16_f32 v121, v116, v117
	global_store_dwordx4 v160, v[118:121], s[44:45] offset:256
	s_waitcnt vmcnt(12)
	v_pk_fma_f32 v[110:111], v[110:111], v[130:131], v[190:191]
	v_pk_fma_f32 v[112:113], v[112:113], v[132:133], v[192:193]
	v_pk_fma_f32 v[106:107], v[106:107], v[134:135], v[194:195]
	v_pk_fma_f32 v[108:109], v[108:109], v[136:137], v[196:197]
	s_add_u32 s42, s42, 0xa0000
	s_addc_u32 s43, s43, 0
	global_load_dwordx4 v[190:193], v161, s[42:43] offset:0
	global_load_dwordx4 v[194:197], v161, s[42:43] offset:16
	v_cvt_pk_bf16_f32 v110, v110, v111
	v_cvt_pk_bf16_f32 v111, v112, v113
	v_cvt_pk_bf16_f32 v112, v106, v107
	v_cvt_pk_bf16_f32 v113, v108, v109
	s_add_u32 s44, s44, 0x10000
	s_addc_u32 s45, s45, 0
	global_store_dwordx4 v160, v[110:113], s[44:45] offset:0
	s_waitcnt vmcnt(13)
	v_pk_fma_f32 v[102:103], v[102:103], v[138:139], v[198:199]
	v_pk_fma_f32 v[104:105], v[104:105], v[140:141], v[200:201]
	v_pk_fma_f32 v[98:99], v[98:99], v[142:143], v[202:203]
	v_pk_fma_f32 v[100:101], v[100:101], v[144:145], v[204:205]
	global_load_dwordx4 v[198:201], v161, s[42:43] offset:512
	global_load_dwordx4 v[202:205], v161, s[42:43] offset:528
	v_cvt_pk_bf16_f32 v102, v102, v103
	v_cvt_pk_bf16_f32 v103, v104, v105
	v_cvt_pk_bf16_f32 v104, v98, v99
	v_cvt_pk_bf16_f32 v105, v100, v101
	global_store_dwordx4 v160, v[102:105], s[44:45] offset:256
	s_waitcnt vmcnt(14)
	v_pk_fma_f32 v[94:95], v[94:95], v[130:131], v[206:207]
	v_pk_fma_f32 v[96:97], v[96:97], v[132:133], v[208:209]
	v_pk_fma_f32 v[90:91], v[90:91], v[134:135], v[216:217]
	v_pk_fma_f32 v[92:93], v[92:93], v[136:137], v[218:219]
	s_add_u32 s42, s42, 0x20000
	s_addc_u32 s43, s43, 0
	global_load_dwordx4 v[206:209], v161, s[42:43] offset:0
	global_load_dwordx4 v[216:219], v161, s[42:43] offset:16
	v_cvt_pk_bf16_f32 v94, v94, v95
	v_cvt_pk_bf16_f32 v95, v96, v97
	v_cvt_pk_bf16_f32 v96, v90, v91
	v_cvt_pk_bf16_f32 v97, v92, v93
	s_add_u32 s44, s44, 0x10000
	s_addc_u32 s45, s45, 0
	global_store_dwordx4 v160, v[94:97], s[44:45] offset:0
	s_waitcnt vmcnt(15)
	v_pk_fma_f32 v[86:87], v[86:87], v[138:139], v[226:227]
	v_pk_fma_f32 v[88:89], v[88:89], v[140:141], v[228:229]
	v_pk_fma_f32 v[82:83], v[82:83], v[142:143], v[230:231]
	v_pk_fma_f32 v[84:85], v[84:85], v[144:145], v[232:233]
	global_load_dwordx4 v[226:229], v161, s[42:43] offset:512
	global_load_dwordx4 v[230:233], v161, s[42:43] offset:528
	v_cvt_pk_bf16_f32 v86, v86, v87
	v_cvt_pk_bf16_f32 v87, v88, v89
	v_cvt_pk_bf16_f32 v88, v82, v83
	v_cvt_pk_bf16_f32 v89, v84, v85
	global_store_dwordx4 v160, v[86:89], s[44:45] offset:256
	s_waitcnt vmcnt(16)
; __device__ __forceinline__ unsigned pk2(float lo, float hi) { return f2bf(lo) | (f2bf(hi) << 16); }
;     __device__ __forceinline__ void epi(const f32x4 (&acc)[2][2][4][2], const Unit& u, int wr, int wc, int fr, int fq) const {
;     ...
;         for (int ai = 0; ai < 2; ++ai)
; #pragma unroll
;             for (int m = 0; m < 4; ++m) { const size_t ro = (size_t)(ai * 128 + m * 16) * DM;
; #pragma unroll
;                 for (int bj = 0; bj < 2; ++bj) { const int cofs = bj * 128;
;                     const f32x4 g0 = *(const f32x4*)(g1 + cofs * 4 + lcol * 4), g1v = *(const f32x4*)(g1 + cofs * 4 + lcol * 4 + 16);
;                     f32x4 x0, x1v;
;                     if (f32in) { x0 = *(const f32x4*)(xin + (ro + cofs) * 4 + loff4); x1v = *(const f32x4*)(xin + (ro + cofs) * 4 + loff4 + 16); }
;                     else { const u32x4 w = *(const u32x4*)(xin + (ro + cofs) * 2 + loff2); x0 = (f32x4){bflo(w.x), bfhi(w.x), bflo(w.y), bfhi(w.y)}; x1v = (f32x4){bflo(w.z), bfhi(w.z), bflo(w.w), bfhi(w.w)}; }
;                     const f32x4 o0 = x0 + g0 * acc[ai][bj][m][0], o1 = x1v + g1v * acc[ai][bj][m][1];
;                     u32x4 ow; ow.x = pk2(o0[0], o0[1]); ow.y = pk2(o0[2], o0[3]); ow.z = pk2(o1[0], o1[1]); ow.w = pk2(o1[2], o1[3]);
;                     *(u32x4*)(xo + (ro + cofs) * 2 + loff2) = ow; }
;                 asm volatile("" ::: "memory"); }
	v_pk_fma_f32 v[78:79], v[78:79], v[130:131], v[172:173]
	v_pk_fma_f32 v[80:81], v[80:81], v[132:133], v[174:175]
	v_pk_fma_f32 v[74:75], v[74:75], v[134:135], v[176:177]
	v_pk_fma_f32 v[76:77], v[76:77], v[136:137], v[178:179]
	s_add_u32 s42, s42, 0x20000
	s_addc_u32 s43, s43, 0
	global_load_dwordx4 v[172:175], v161, s[42:43] offset:0
	global_load_dwordx4 v[176:179], v161, s[42:43] offset:16
	v_cvt_pk_bf16_f32 v78, v78, v79
	v_cvt_pk_bf16_f32 v79, v80, v81
	v_cvt_pk_bf16_f32 v80, v74, v75
	v_cvt_pk_bf16_f32 v81, v76, v77
	s_add_u32 s44, s44, 0x10000
	s_addc_u32 s45, s45, 0
	global_store_dwordx4 v160, v[78:81], s[44:45] offset:0
	s_waitcnt vmcnt(16)
	v_pk_fma_f32 v[70:71], v[70:71], v[138:139], v[182:183]
	v_pk_fma_f32 v[72:73], v[72:73], v[140:141], v[184:185]
	v_pk_fma_f32 v[66:67], v[66:67], v[142:143], v[186:187]
	v_pk_fma_f32 v[68:69], v[68:69], v[144:145], v[188:189]
	global_load_dwordx4 v[182:185], v161, s[42:43] offset:512
	global_load_dwordx4 v[186:189], v161, s[42:43] offset:528
	v_cvt_pk_bf16_f32 v70, v70, v71
	v_cvt_pk_bf16_f32 v71, v72, v73
	v_cvt_pk_bf16_f32 v72, v66, v67
	v_cvt_pk_bf16_f32 v73, v68, v69
	global_store_dwordx4 v160, v[70:73], s[44:45] offset:256
	s_waitcnt vmcnt(16)
	v_pk_fma_f32 v[62:63], v[62:63], v[130:131], v[190:191]
	v_pk_fma_f32 v[64:65], v[64:65], v[132:133], v[192:193]
	v_pk_fma_f32 v[58:59], v[58:59], v[134:135], v[194:195]
	v_pk_fma_f32 v[60:61], v[60:61], v[136:137], v[196:197]
	s_add_u32 s42, s42, 0x20000
	s_addc_u32 s43, s43, 0
	global_load_dwordx4 v[190:193], v161, s[42:43] offset:0
	global_load_dwordx4 v[194:197], v161, s[42:43] offset:16
	v_cvt_pk_bf16_f32 v62, v62, v63
	v_cvt_pk_bf16_f32 v63, v64, v65
	v_cvt_pk_bf16_f32 v64, v58, v59
	v_cvt_pk_bf16_f32 v65, v60, v61
	s_add_u32 s44, s44, 0x50000
	s_addc_u32 s45, s45, 0
	global_store_dwordx4 v160, v[62:65], s[44:45] offset:0
	s_waitcnt vmcnt(16)
	v_pk_fma_f32 v[54:55], v[54:55], v[138:139], v[198:199]
	v_pk_fma_f32 v[56:57], v[56:57], v[140:141], v[200:201]
	v_pk_fma_f32 v[50:51], v[50:51], v[142:143], v[202:203]
	v_pk_fma_f32 v[52:53], v[52:53], v[144:145], v[204:205]
	global_load_dwordx4 v[198:201], v161, s[42:43] offset:512
	global_load_dwordx4 v[202:205], v161, s[42:43] offset:528
	v_cvt_pk_bf16_f32 v54, v54, v55
	v_cvt_pk_bf16_f32 v55, v56, v57
	v_cvt_pk_bf16_f32 v56, v50, v51
	v_cvt_pk_bf16_f32 v57, v52, v53
	global_store_dwordx4 v160, v[54:57], s[44:45] offset:256
	s_waitcnt vmcnt(16)
	v_pk_fma_f32 v[46:47], v[46:47], v[130:131], v[206:207]
	v_pk_fma_f32 v[48:49], v[48:49], v[132:133], v[208:209]
	v_pk_fma_f32 v[42:43], v[42:43], v[134:135], v[216:217]
	v_pk_fma_f32 v[44:45], v[44:45], v[136:137], v[218:219]
	v_cvt_pk_bf16_f32 v46, v46, v47
	v_cvt_pk_bf16_f32 v47, v48, v49
	v_cvt_pk_bf16_f32 v48, v42, v43
	v_cvt_pk_bf16_f32 v49, v44, v45
	s_add_u32 s44, s44, 0x10000
	s_addc_u32 s45, s45, 0
	global_store_dwordx4 v160, v[46:49], s[44:45] offset:0
	s_waitcnt vmcnt(14)
	v_pk_fma_f32 v[38:39], v[38:39], v[138:139], v[226:227]
	v_pk_fma_f32 v[40:41], v[40:41], v[140:141], v[228:229]
	v_pk_fma_f32 v[34:35], v[34:35], v[142:143], v[230:231]
	v_pk_fma_f32 v[36:37], v[36:37], v[144:145], v[232:233]
	v_cvt_pk_bf16_f32 v38, v38, v39
	v_cvt_pk_bf16_f32 v39, v40, v41
	v_cvt_pk_bf16_f32 v40, v34, v35
	v_cvt_pk_bf16_f32 v41, v36, v37
	global_store_dwordx4 v160, v[38:41], s[44:45] offset:256
	s_waitcnt vmcnt(12)
	v_pk_fma_f32 v[30:31], v[30:31], v[130:131], v[172:173]
	v_pk_fma_f32 v[32:33], v[32:33], v[132:133], v[174:175]
	v_pk_fma_f32 v[26:27], v[26:27], v[134:135], v[176:177]
	v_pk_fma_f32 v[28:29], v[28:29], v[136:137], v[178:179]
	v_cvt_pk_bf16_f32 v30, v30, v31
	v_cvt_pk_bf16_f32 v31, v32, v33
	v_cvt_pk_bf16_f32 v32, v26, v27
	v_cvt_pk_bf16_f32 v33, v28, v29
	s_add_u32 s44, s44, 0x10000
	s_addc_u32 s45, s45, 0
	global_store_dwordx4 v160, v[30:33], s[44:45] offset:0
	s_waitcnt vmcnt(10)
	v_pk_fma_f32 v[22:23], v[22:23], v[138:139], v[182:183]
	v_pk_fma_f32 v[24:25], v[24:25], v[140:141], v[184:185]
	v_pk_fma_f32 v[18:19], v[18:19], v[142:143], v[186:187]
	v_pk_fma_f32 v[20:21], v[20:21], v[144:145], v[188:189]
	v_cvt_pk_bf16_f32 v22, v22, v23
	v_cvt_pk_bf16_f32 v23, v24, v25
	v_cvt_pk_bf16_f32 v24, v18, v19
	v_cvt_pk_bf16_f32 v25, v20, v21
	global_store_dwordx4 v160, v[22:25], s[44:45] offset:256
	s_waitcnt vmcnt(8)
	v_pk_fma_f32 v[14:15], v[14:15], v[130:131], v[190:191]
	v_pk_fma_f32 v[16:17], v[16:17], v[132:133], v[192:193]
	v_pk_fma_f32 v[10:11], v[10:11], v[134:135], v[194:195]
	v_pk_fma_f32 v[12:13], v[12:13], v[136:137], v[196:197]
	v_cvt_pk_bf16_f32 v14, v14, v15
	v_cvt_pk_bf16_f32 v15, v16, v17
	v_cvt_pk_bf16_f32 v16, v10, v11
	v_cvt_pk_bf16_f32 v17, v12, v13
	s_add_u32 s44, s44, 0x10000
	s_addc_u32 s45, s45, 0
	global_store_dwordx4 v160, v[14:17], s[44:45] offset:0
	s_waitcnt vmcnt(6)
	v_pk_fma_f32 v[6:7], v[6:7], v[138:139], v[198:199]
	v_pk_fma_f32 v[8:9], v[8:9], v[140:141], v[200:201]
	v_pk_fma_f32 v[2:3], v[2:3], v[142:143], v[202:203]
	v_pk_fma_f32 v[4:5], v[4:5], v[144:145], v[204:205]
	v_cvt_pk_bf16_f32 v6, v6, v7
	v_cvt_pk_bf16_f32 v7, v8, v9
	v_cvt_pk_bf16_f32 v8, v2, v3
	v_cvt_pk_bf16_f32 v9, v4, v5
	global_store_dwordx4 v160, v[6:9], s[44:45] offset:256
	s_branch .Lmx_done
; __device__ __forceinline__ unsigned pk2(float lo, float hi) { return f2bf(lo) | (f2bf(hi) << 16); }
;     __device__ __forceinline__ void epi(const f32x4 (&acc)[2][2][4][2], const Unit& u, int wr, int wc, int fr, int fq) const {
;     ...
;         for (int ai = 0; ai < 2; ++ai)
; #pragma unroll
;             for (int m = 0; m < 4; ++m) { const size_t ro = (size_t)(ai * 128 + m * 16) * DM;
; #pragma unroll
;                 for (int bj = 0; bj < 2; ++bj) { const int cofs = bj * 128;
;                     const f32x4 g0 = *(const f32x4*)(g1 + cofs * 4 + lcol * 4), g1v = *(const f32x4*)(g1 + cofs * 4 + lcol * 4 + 16);
;                     f32x4 x0, x1v;
;                     if (f32in) { x0 = *(const f32x4*)(xin + (ro + cofs) * 4 + loff4); x1v = *(const f32x4*)(xin + (ro + cofs) * 4 + loff4 + 16); }
;                     else { const u32x4 w = *(const u32x4*)(xin + (ro + cofs) * 2 + loff2); x0 = (f32x4){bflo(w.x), bfhi(w.x), bflo(w.y), bfhi(w.y)}; x1v = (f32x4){bflo(w.z), bfhi(w.z), bflo(w.w), bfhi(w.w)}; }
;                     const f32x4 o0 = x0 + g0 * acc[ai][bj][m][0], o1 = x1v + g1v * acc[ai][bj][m][1];
;                     u32x4 ow; ow.x = pk2(o0[0], o0[1]); ow.y = pk2(o0[2], o0[3]); ow.z = pk2(o1[0], o1[1]); ow.w = pk2(o1[2], o1[3]);
;                     *(u32x4*)(xo + (ro + cofs) * 2 + loff2) = ow; }
;                 asm volatile("" ::: "memory"); }
.Lmx_bf16:
	v_mov_b32_e32 v161, v160
	s_lshl_b32 s12, s24, 20
	s_lshl_b32 s17, s26, 9
	s_add_i32 s12, s12, s17
	s_add_u32 s42, s67, s12
	s_addc_u32 s43, s68, 0
	global_load_dwordx4 v[172:175], v161, s[42:43] offset:0
	global_load_dwordx4 v[176:179], v161, s[42:43] offset:256
	s_add_u32 s42, s42, 0x10000
	s_addc_u32 s43, s43, 0
	global_load_dwordx4 v[182:185], v161, s[42:43] offset:0
	global_load_dwordx4 v[186:189], v161, s[42:43] offset:256
	s_add_u32 s42, s42, 0x10000
	s_addc_u32 s43, s43, 0
	global_load_dwordx4 v[190:193], v161, s[42:43] offset:0
	global_load_dwordx4 v[194:197], v161, s[42:43] offset:256
	s_add_u32 s42, s42, 0x10000
	s_addc_u32 s43, s43, 0
	global_load_dwordx4 v[198:201], v161, s[42:43] offset:0
	global_load_dwordx4 v[202:205], v161, s[42:43] offset:256
	s_add_u32 s42, s42, 0x50000
	s_addc_u32 s43, s43, 0
	global_load_dwordx4 v[206:209], v161, s[42:43] offset:0
	global_load_dwordx4 v[216:219], v161, s[42:43] offset:256
	s_add_u32 s42, s42, 0x10000
	s_addc_u32 s43, s43, 0
	global_load_dwordx4 v[226:229], v161, s[42:43] offset:0
	global_load_dwordx4 v[230:233], v161, s[42:43] offset:256
	s_waitcnt vmcnt(11)
	v_lshlrev_b32_e32 v162, 16, v172
	v_and_b32_e32 v163, 0xffff0000, v172
	v_lshlrev_b32_e32 v164, 16, v173
	v_and_b32_e32 v165, 0xffff0000, v173
	v_lshlrev_b32_e32 v166, 16, v174
	v_and_b32_e32 v167, 0xffff0000, v174
	v_lshlrev_b32_e32 v222, 16, v175
	v_and_b32_e32 v223, 0xffff0000, v175
	v_pk_fma_f32 v[126:127], v[126:127], v[130:131], v[162:163]
	v_pk_fma_f32 v[128:129], v[128:129], v[132:133], v[164:165]
	v_pk_fma_f32 v[122:123], v[122:123], v[134:135], v[166:167]
	v_pk_fma_f32 v[124:125], v[124:125], v[136:137], v[222:223]
	s_add_u32 s42, s42, 0x10000
	s_addc_u32 s43, s43, 0
	global_load_dwordx4 v[172:175], v161, s[42:43] offset:0
	v_cvt_pk_bf16_f32 v126, v126, v127
	v_cvt_pk_bf16_f32 v127, v128, v129
	v_cvt_pk_bf16_f32 v128, v122, v123
	v_cvt_pk_bf16_f32 v129, v124, v125
	global_store_dwordx4 v160, v[126:129], s[44:45] offset:0
	s_waitcnt vmcnt(12)
	v_lshlrev_b32_e32 v162, 16, v176
	v_and_b32_e32 v163, 0xffff0000, v176
	v_lshlrev_b32_e32 v164, 16, v177
	v_and_b32_e32 v165, 0xffff0000, v177
	v_lshlrev_b32_e32 v166, 16, v178
	v_and_b32_e32 v167, 0xffff0000, v178
	v_lshlrev_b32_e32 v222, 16, v179
	v_and_b32_e32 v223, 0xffff0000, v179
	v_pk_fma_f32 v[118:119], v[118:119], v[138:139], v[162:163]
	v_pk_fma_f32 v[120:121], v[120:121], v[140:141], v[164:165]
	v_pk_fma_f32 v[114:115], v[114:115], v[142:143], v[166:167]
	v_pk_fma_f32 v[116:117], v[116:117], v[144:145], v[222:223]
	global_load_dwordx4 v[176:179], v161, s[42:43] offset:256
	v_cvt_pk_bf16_f32 v118, v118, v119
	v_cvt_pk_bf16_f32 v119, v120, v121
	v_cvt_pk_bf16_f32 v120, v114, v115
	v_cvt_pk_bf16_f32 v121, v116, v117
	global_store_dwordx4 v160, v[118:121], s[44:45] offset:256
	s_waitcnt vmcnt(13)
	v_lshlrev_b32_e32 v162, 16, v182
	v_and_b32_e32 v163, 0xffff0000, v182
	v_lshlrev_b32_e32 v164, 16, v183
	v_and_b32_e32 v165, 0xffff0000, v183
	v_lshlrev_b32_e32 v166, 16, v184
	v_and_b32_e32 v167, 0xffff0000, v184
	v_lshlrev_b32_e32 v222, 16, v185
	v_and_b32_e32 v223, 0xffff0000, v185
	v_pk_fma_f32 v[110:111], v[110:111], v[130:131], v[162:163]
	v_pk_fma_f32 v[112:113], v[112:113], v[132:133], v[164:165]
	v_pk_fma_f32 v[106:107], v[106:107], v[134:135], v[166:167]
	v_pk_fma_f32 v[108:109], v[108:109], v[136:137], v[222:223]
	s_add_u32 s42, s42, 0x10000
	s_addc_u32 s43, s43, 0
	global_load_dwordx4 v[182:185], v161, s[42:43] offset:0
	v_cvt_pk_bf16_f32 v110, v110, v111
	v_cvt_pk_bf16_f32 v111, v112, v113
	v_cvt_pk_bf16_f32 v112, v106, v107
	v_cvt_pk_bf16_f32 v113, v108, v109
	s_add_u32 s44, s44, 0x10000
	s_addc_u32 s45, s45, 0
	global_store_dwordx4 v160, v[110:113], s[44:45] offset:0
	s_waitcnt vmcnt(14)
	v_lshlrev_b32_e32 v162, 16, v186
	v_and_b32_e32 v163, 0xffff0000, v186
	v_lshlrev_b32_e32 v164, 16, v187
	v_and_b32_e32 v165, 0xffff0000, v187
	v_lshlrev_b32_e32 v166, 16, v188
	v_and_b32_e32 v167, 0xffff0000, v188
	v_lshlrev_b32_e32 v222, 16, v189
	v_and_b32_e32 v223, 0xffff0000, v189
	v_pk_fma_f32 v[102:103], v[102:103], v[138:139], v[162:163]
	v_pk_fma_f32 v[104:105], v[104:105], v[140:141], v[164:165]
	v_pk_fma_f32 v[98:99], v[98:99], v[142:143], v[166:167]
	v_pk_fma_f32 v[100:101], v[100:101], v[144:145], v[222:223]
	global_load_dwordx4 v[186:189], v161, s[42:43] offset:256
	v_cvt_pk_bf16_f32 v102, v102, v103
	v_cvt_pk_bf16_f32 v103, v104, v105
	v_cvt_pk_bf16_f32 v104, v98, v99
	v_cvt_pk_bf16_f32 v105, v100, v101
	global_store_dwordx4 v160, v[102:105], s[44:45] offset:256
	s_waitcnt vmcnt(15)
	v_lshlrev_b32_e32 v162, 16, v190
	v_and_b32_e32 v163, 0xffff0000, v190
	v_lshlrev_b32_e32 v164, 16, v191
	v_and_b32_e32 v165, 0xffff0000, v191
	v_lshlrev_b32_e32 v166, 16, v192
	v_and_b32_e32 v167, 0xffff0000, v192
	v_lshlrev_b32_e32 v222, 16, v193
	v_and_b32_e32 v223, 0xffff0000, v193
	v_pk_fma_f32 v[94:95], v[94:95], v[130:131], v[162:163]
	v_pk_fma_f32 v[96:97], v[96:97], v[132:133], v[164:165]
	v_pk_fma_f32 v[90:91], v[90:91], v[134:135], v[166:167]
	v_pk_fma_f32 v[92:93], v[92:93], v[136:137], v[222:223]
	v_cvt_pk_bf16_f32 v94, v94, v95
	v_cvt_pk_bf16_f32 v95, v96, v97
	v_cvt_pk_bf16_f32 v96, v90, v91
	v_cvt_pk_bf16_f32 v97, v92, v93
	s_add_u32 s44, s44, 0x10000
	s_addc_u32 s45, s45, 0
	global_store_dwordx4 v160, v[94:97], s[44:45] offset:0
	s_waitcnt vmcnt(15)
; __device__ __forceinline__ unsigned pk2(float lo, float hi) { return f2bf(lo) | (f2bf(hi) << 16); }
;     __device__ __forceinline__ void epi(const f32x4 (&acc)[2][2][4][2], const Unit& u, int wr, int wc, int fr, int fq) const {
;     ...
;         for (int ai = 0; ai < 2; ++ai)
; #pragma unroll
;             for (int m = 0; m < 4; ++m) { const size_t ro = (size_t)(ai * 128 + m * 16) * DM;
; #pragma unroll
;                 for (int bj = 0; bj < 2; ++bj) { const int cofs = bj * 128;
;                     const f32x4 g0 = *(const f32x4*)(g1 + cofs * 4 + lcol * 4), g1v = *(const f32x4*)(g1 + cofs * 4 + lcol * 4 + 16);
;                     f32x4 x0, x1v;
;                     if (f32in) { x0 = *(const f32x4*)(xin + (ro + cofs) * 4 + loff4); x1v = *(const f32x4*)(xin + (ro + cofs) * 4 + loff4 + 16); }
;                     else { const u32x4 w = *(const u32x4*)(xin + (ro + cofs) * 2 + loff2); x0 = (f32x4){bflo(w.x), bfhi(w.x), bflo(w.y), bfhi(w.y)}; x1v = (f32x4){bflo(w.z), bfhi(w.z), bflo(w.w), bfhi(w.w)}; }
;                     const f32x4 o0 = x0 + g0 * acc[ai][bj][m][0], o1 = x1v + g1v * acc[ai][bj][m][1];
;                     u32x4 ow; ow.x = pk2(o0[0], o0[1]); ow.y = pk2(o0[2], o0[3]); ow.z = pk2(o1[0], o1[1]); ow.w = pk2(o1[2], o1[3]);
;                     *(u32x4*)(xo + (ro + cofs) * 2 + loff2) = ow; }
;                 asm volatile("" ::: "memory"); }
	v_lshlrev_b32_e32 v162, 16, v194
	v_and_b32_e32 v163, 0xffff0000, v194
	v_lshlrev_b32_e32 v164, 16, v195
	v_and_b32_e32 v165, 0xffff0000, v195
	v_lshlrev_b32_e32 v166, 16, v196
	v_and_b32_e32 v167, 0xffff0000, v196
	v_lshlrev_b32_e32 v222, 16, v197
	v_and_b32_e32 v223, 0xffff0000, v197
	v_pk_fma_f32 v[86:87], v[86:87], v[138:139], v[162:163]
	v_pk_fma_f32 v[88:89], v[88:89], v[140:141], v[164:165]
	v_pk_fma_f32 v[82:83], v[82:83], v[142:143], v[166:167]
	v_pk_fma_f32 v[84:85], v[84:85], v[144:145], v[222:223]
	v_cvt_pk_bf16_f32 v86, v86, v87
	v_cvt_pk_bf16_f32 v87, v88, v89
	v_cvt_pk_bf16_f32 v88, v82, v83
	v_cvt_pk_bf16_f32 v89, v84, v85
	global_store_dwordx4 v160, v[86:89], s[44:45] offset:256
	s_waitcnt vmcnt(15)
	v_lshlrev_b32_e32 v162, 16, v198
	v_and_b32_e32 v163, 0xffff0000, v198
	v_lshlrev_b32_e32 v164, 16, v199
	v_and_b32_e32 v165, 0xffff0000, v199
	v_lshlrev_b32_e32 v166, 16, v200
	v_and_b32_e32 v167, 0xffff0000, v200
	v_lshlrev_b32_e32 v222, 16, v201
	v_and_b32_e32 v223, 0xffff0000, v201
	v_pk_fma_f32 v[78:79], v[78:79], v[130:131], v[162:163]
	v_pk_fma_f32 v[80:81], v[80:81], v[132:133], v[164:165]
	v_pk_fma_f32 v[74:75], v[74:75], v[134:135], v[166:167]
	v_pk_fma_f32 v[76:77], v[76:77], v[136:137], v[222:223]
	v_cvt_pk_bf16_f32 v78, v78, v79
	v_cvt_pk_bf16_f32 v79, v80, v81
	v_cvt_pk_bf16_f32 v80, v74, v75
	v_cvt_pk_bf16_f32 v81, v76, v77
	s_add_u32 s44, s44, 0x10000
	s_addc_u32 s45, s45, 0
	global_store_dwordx4 v160, v[78:81], s[44:45] offset:0
	s_waitcnt vmcnt(15)
	v_lshlrev_b32_e32 v162, 16, v202
	v_and_b32_e32 v163, 0xffff0000, v202
	v_lshlrev_b32_e32 v164, 16, v203
	v_and_b32_e32 v165, 0xffff0000, v203
	v_lshlrev_b32_e32 v166, 16, v204
	v_and_b32_e32 v167, 0xffff0000, v204
	v_lshlrev_b32_e32 v222, 16, v205
	v_and_b32_e32 v223, 0xffff0000, v205
	v_pk_fma_f32 v[70:71], v[70:71], v[138:139], v[162:163]
	v_pk_fma_f32 v[72:73], v[72:73], v[140:141], v[164:165]
	v_pk_fma_f32 v[66:67], v[66:67], v[142:143], v[166:167]
	v_pk_fma_f32 v[68:69], v[68:69], v[144:145], v[222:223]
	v_cvt_pk_bf16_f32 v70, v70, v71
	v_cvt_pk_bf16_f32 v71, v72, v73
	v_cvt_pk_bf16_f32 v72, v66, v67
	v_cvt_pk_bf16_f32 v73, v68, v69
	global_store_dwordx4 v160, v[70:73], s[44:45] offset:256
	s_waitcnt vmcnt(15)
	v_lshlrev_b32_e32 v162, 16, v206
	v_and_b32_e32 v163, 0xffff0000, v206
	v_lshlrev_b32_e32 v164, 16, v207
	v_and_b32_e32 v165, 0xffff0000, v207
	v_lshlrev_b32_e32 v166, 16, v208
	v_and_b32_e32 v167, 0xffff0000, v208
	v_lshlrev_b32_e32 v222, 16, v209
	v_and_b32_e32 v223, 0xffff0000, v209
	v_pk_fma_f32 v[62:63], v[62:63], v[130:131], v[162:163]
	v_pk_fma_f32 v[64:65], v[64:65], v[132:133], v[164:165]
	v_pk_fma_f32 v[58:59], v[58:59], v[134:135], v[166:167]
	v_pk_fma_f32 v[60:61], v[60:61], v[136:137], v[222:223]
	v_cvt_pk_bf16_f32 v62, v62, v63
	v_cvt_pk_bf16_f32 v63, v64, v65
	v_cvt_pk_bf16_f32 v64, v58, v59
	v_cvt_pk_bf16_f32 v65, v60, v61
	s_add_u32 s44, s44, 0x50000
	s_addc_u32 s45, s45, 0
	global_store_dwordx4 v160, v[62:65], s[44:45] offset:0
	s_waitcnt vmcnt(15)
	v_lshlrev_b32_e32 v162, 16, v216
	v_and_b32_e32 v163, 0xffff0000, v216
	v_lshlrev_b32_e32 v164, 16, v217
	v_and_b32_e32 v165, 0xffff0000, v217
	v_lshlrev_b32_e32 v166, 16, v218
	v_and_b32_e32 v167, 0xffff0000, v218
	v_lshlrev_b32_e32 v222, 16, v219
	v_and_b32_e32 v223, 0xffff0000, v219
	v_pk_fma_f32 v[54:55], v[54:55], v[138:139], v[162:163]
	v_pk_fma_f32 v[56:57], v[56:57], v[140:141], v[164:165]
	v_pk_fma_f32 v[50:51], v[50:51], v[142:143], v[166:167]
	v_pk_fma_f32 v[52:53], v[52:53], v[144:145], v[222:223]
	v_cvt_pk_bf16_f32 v54, v54, v55
	v_cvt_pk_bf16_f32 v55, v56, v57
	v_cvt_pk_bf16_f32 v56, v50, v51
	v_cvt_pk_bf16_f32 v57, v52, v53
	global_store_dwordx4 v160, v[54:57], s[44:45] offset:256
	s_waitcnt vmcnt(15)
	v_lshlrev_b32_e32 v162, 16, v226
	v_and_b32_e32 v163, 0xffff0000, v226
	v_lshlrev_b32_e32 v164, 16, v227
	v_and_b32_e32 v165, 0xffff0000, v227
	v_lshlrev_b32_e32 v166, 16, v228
	v_and_b32_e32 v167, 0xffff0000, v228
	v_lshlrev_b32_e32 v222, 16, v229
	v_and_b32_e32 v223, 0xffff0000, v229
	v_pk_fma_f32 v[46:47], v[46:47], v[130:131], v[162:163]
	v_pk_fma_f32 v[48:49], v[48:49], v[132:133], v[164:165]
	v_pk_fma_f32 v[42:43], v[42:43], v[134:135], v[166:167]
	v_pk_fma_f32 v[44:45], v[44:45], v[136:137], v[222:223]
	v_cvt_pk_bf16_f32 v46, v46, v47
	v_cvt_pk_bf16_f32 v47, v48, v49
	v_cvt_pk_bf16_f32 v48, v42, v43
	v_cvt_pk_bf16_f32 v49, v44, v45
	s_add_u32 s44, s44, 0x10000
	s_addc_u32 s45, s45, 0
	global_store_dwordx4 v160, v[46:49], s[44:45] offset:0
	s_waitcnt vmcnt(15)
	v_lshlrev_b32_e32 v162, 16, v230
	v_and_b32_e32 v163, 0xffff0000, v230
	v_lshlrev_b32_e32 v164, 16, v231
	v_and_b32_e32 v165, 0xffff0000, v231
	v_lshlrev_b32_e32 v166, 16, v232
	v_and_b32_e32 v167, 0xffff0000, v232
	v_lshlrev_b32_e32 v222, 16, v233
	v_and_b32_e32 v223, 0xffff0000, v233
	v_pk_fma_f32 v[38:39], v[38:39], v[138:139], v[162:163]
	v_pk_fma_f32 v[40:41], v[40:41], v[140:141], v[164:165]
	v_pk_fma_f32 v[34:35], v[34:35], v[142:143], v[166:167]
	v_pk_fma_f32 v[36:37], v[36:37], v[144:145], v[222:223]
	v_cvt_pk_bf16_f32 v38, v38, v39
	v_cvt_pk_bf16_f32 v39, v40, v41
	v_cvt_pk_bf16_f32 v40, v34, v35
	v_cvt_pk_bf16_f32 v41, v36, v37
	global_store_dwordx4 v160, v[38:41], s[44:45] offset:256
	s_waitcnt vmcnt(15)
	v_lshlrev_b32_e32 v162, 16, v172
	v_and_b32_e32 v163, 0xffff0000, v172
	v_lshlrev_b32_e32 v164, 16, v173
	v_and_b32_e32 v165, 0xffff0000, v173
	v_lshlrev_b32_e32 v166, 16, v174
	v_and_b32_e32 v167, 0xffff0000, v174
	v_lshlrev_b32_e32 v222, 16, v175
	v_and_b32_e32 v223, 0xffff0000, v175
	v_pk_fma_f32 v[30:31], v[30:31], v[130:131], v[162:163]
	v_pk_fma_f32 v[32:33], v[32:33], v[132:133], v[164:165]
	v_pk_fma_f32 v[26:27], v[26:27], v[134:135], v[166:167]
	v_pk_fma_f32 v[28:29], v[28:29], v[136:137], v[222:223]
	v_cvt_pk_bf16_f32 v30, v30, v31
	v_cvt_pk_bf16_f32 v31, v32, v33
	v_cvt_pk_bf16_f32 v32, v26, v27
	v_cvt_pk_bf16_f32 v33, v28, v29
	s_add_u32 s44, s44, 0x10000
	s_addc_u32 s45, s45, 0
	global_store_dwordx4 v160, v[30:33], s[44:45] offset:0
	s_waitcnt vmcnt(14)
; __device__ __forceinline__ unsigned pk2(float lo, float hi) { return f2bf(lo) | (f2bf(hi) << 16); }
; #define PG8_WAIT_V(n) asm volatile("s_waitcnt vmcnt(" #n ")" ::: "memory")
; #define PG8_BAR __builtin_amdgcn_s_barrier()
; template <class P>
; __device__ __forceinline__ void gemm_phase(LAS unsigned char* lds, const P& p) {
;     ...
;         if (!has_next) break;
; #pragma unroll
;         for (int a = 0; a < 2; ++a)
; #pragma unroll
;             for (int b = 0; b < 2; ++b)
; #pragma unroll
;                 for (int m = 0; m < 4; ++m)
; #pragma unroll
;                     for (int n = 0; n < 2; ++n) acc[a][b][m][n] = (f32x4){0.f, 0.f, 0.f, 0.f};
;         cur = nxt; cA = nA; cB = nB; ++ui;
;         if (wr == 1) PG8_BAR;
;     }
;     PG8_WAIT_V(0);
;     PG8_BAR;
;     __device__ __forceinline__ void epi(const f32x4 (&acc)[2][2][4][2], const Unit& u, int wr, int wc, int fr, int fq) const {
;     ...
;         for (int ai = 0; ai < 2; ++ai)
; #pragma unroll
;             for (int m = 0; m < 4; ++m) { const size_t ro = (size_t)(ai * 128 + m * 16) * DM;
; #pragma unroll
;                 for (int bj = 0; bj < 2; ++bj) { const int cofs = bj * 128;
;                     const f32x4 g0 = *(const f32x4*)(g1 + cofs * 4 + lcol * 4), g1v = *(const f32x4*)(g1 + cofs * 4 + lcol * 4 + 16);
;                     f32x4 x0, x1v;
;                     if (f32in) { x0 = *(const f32x4*)(xin + (ro + cofs) * 4 + loff4); x1v = *(const f32x4*)(xin + (ro + cofs) * 4 + loff4 + 16); }
;                     else { const u32x4 w = *(const u32x4*)(xin + (ro + cofs) * 2 + loff2); x0 = (f32x4){bflo(w.x), bfhi(w.x), bflo(w.y), bfhi(w.y)}; x1v = (f32x4){bflo(w.z), bfhi(w.z), bflo(w.w), bfhi(w.w)}; }
;                     const f32x4 o0 = x0 + g0 * acc[ai][bj][m][0], o1 = x1v + g1v * acc[ai][bj][m][1];
;                     u32x4 ow; ow.x = pk2(o0[0], o0[1]); ow.y = pk2(o0[2], o0[3]); ow.z = pk2(o1[0], o1[1]); ow.w = pk2(o1[2], o1[3]);
;                     *(u32x4*)(xo + (ro + cofs) * 2 + loff2) = ow; }
;                 asm volatile("" ::: "memory"); }
	v_lshlrev_b32_e32 v162, 16, v176
	v_and_b32_e32 v163, 0xffff0000, v176
	v_lshlrev_b32_e32 v164, 16, v177
	v_and_b32_e32 v165, 0xffff0000, v177
	v_lshlrev_b32_e32 v166, 16, v178
	v_and_b32_e32 v167, 0xffff0000, v178
	v_lshlrev_b32_e32 v222, 16, v179
	v_and_b32_e32 v223, 0xffff0000, v179
	v_pk_fma_f32 v[22:23], v[22:23], v[138:139], v[162:163]
	v_pk_fma_f32 v[24:25], v[24:25], v[140:141], v[164:165]
	v_pk_fma_f32 v[18:19], v[18:19], v[142:143], v[166:167]
	v_pk_fma_f32 v[20:21], v[20:21], v[144:145], v[222:223]
	v_cvt_pk_bf16_f32 v22, v22, v23
	v_cvt_pk_bf16_f32 v23, v24, v25
	v_cvt_pk_bf16_f32 v24, v18, v19
	v_cvt_pk_bf16_f32 v25, v20, v21
	global_store_dwordx4 v160, v[22:25], s[44:45] offset:256
	s_waitcnt vmcnt(13)
	v_lshlrev_b32_e32 v162, 16, v182
	v_and_b32_e32 v163, 0xffff0000, v182
	v_lshlrev_b32_e32 v164, 16, v183
	v_and_b32_e32 v165, 0xffff0000, v183
	v_lshlrev_b32_e32 v166, 16, v184
	v_and_b32_e32 v167, 0xffff0000, v184
	v_lshlrev_b32_e32 v222, 16, v185
	v_and_b32_e32 v223, 0xffff0000, v185
	v_pk_fma_f32 v[14:15], v[14:15], v[130:131], v[162:163]
	v_pk_fma_f32 v[16:17], v[16:17], v[132:133], v[164:165]
	v_pk_fma_f32 v[10:11], v[10:11], v[134:135], v[166:167]
	v_pk_fma_f32 v[12:13], v[12:13], v[136:137], v[222:223]
	v_cvt_pk_bf16_f32 v14, v14, v15
	v_cvt_pk_bf16_f32 v15, v16, v17
	v_cvt_pk_bf16_f32 v16, v10, v11
	v_cvt_pk_bf16_f32 v17, v12, v13
	s_add_u32 s44, s44, 0x10000
	s_addc_u32 s45, s45, 0
	global_store_dwordx4 v160, v[14:17], s[44:45] offset:0
	s_waitcnt vmcnt(12)
	v_lshlrev_b32_e32 v162, 16, v186
	v_and_b32_e32 v163, 0xffff0000, v186
	v_lshlrev_b32_e32 v164, 16, v187
	v_and_b32_e32 v165, 0xffff0000, v187
	v_lshlrev_b32_e32 v166, 16, v188
	v_and_b32_e32 v167, 0xffff0000, v188
	v_lshlrev_b32_e32 v222, 16, v189
	v_and_b32_e32 v223, 0xffff0000, v189
	v_pk_fma_f32 v[6:7], v[6:7], v[138:139], v[162:163]
	v_pk_fma_f32 v[8:9], v[8:9], v[140:141], v[164:165]
	v_pk_fma_f32 v[2:3], v[2:3], v[142:143], v[166:167]
	v_pk_fma_f32 v[4:5], v[4:5], v[144:145], v[222:223]
	v_cvt_pk_bf16_f32 v6, v6, v7
	v_cvt_pk_bf16_f32 v7, v8, v9
	v_cvt_pk_bf16_f32 v8, v2, v3
	v_cvt_pk_bf16_f32 v9, v4, v5
	global_store_dwordx4 v160, v[6:9], s[44:45] offset:256
.Lmx_done:
	s_andn2_b64 vcc, exec, s[38:39]
	s_mov_b64 s[24:25], -1
	s_cbranch_vccnz .LBB0_1761
	s_andn2_b64 vcc, exec, s[4:5]
	s_cbranch_vccnz .LBB0_1760
	s_barrier
	s_branch .LBB0_1760
.LBB0_1827:
	v_mov_b32_e32 v129, 0
	v_mov_b32_e32 v128, v129
	v_mov_b32_e32 v127, v129
	v_mov_b32_e32 v126, v129
	v_mov_b32_e32 v125, v129
	v_mov_b32_e32 v124, v129
	v_mov_b32_e32 v123, v129
	v_mov_b32_e32 v122, v129
	v_mov_b32_e32 v113, v129
	v_mov_b32_e32 v112, v129
	v_mov_b32_e32 v111, v129
	v_mov_b32_e32 v110, v129
	v_mov_b32_e32 v109, v129
	v_mov_b32_e32 v108, v129
	v_mov_b32_e32 v107, v129
	v_mov_b32_e32 v106, v129
	v_mov_b32_e32 v97, v129
	v_mov_b32_e32 v96, v129
	v_mov_b32_e32 v95, v129
	v_mov_b32_e32 v94, v129
	v_mov_b32_e32 v93, v129
	v_mov_b32_e32 v92, v129
	v_mov_b32_e32 v91, v129
	v_mov_b32_e32 v90, v129
	v_mov_b32_e32 v81, v129
	v_mov_b32_e32 v80, v129
	v_mov_b32_e32 v79, v129
	v_mov_b32_e32 v78, v129
	v_mov_b32_e32 v77, v129
	v_mov_b32_e32 v76, v129
	v_mov_b32_e32 v75, v129
	v_mov_b32_e32 v74, v129
	v_mov_b32_e32 v121, v129
	v_mov_b32_e32 v120, v129
	v_mov_b32_e32 v119, v129
	v_mov_b32_e32 v118, v129
	v_mov_b32_e32 v117, v129
	v_mov_b32_e32 v116, v129
	v_mov_b32_e32 v115, v129
	v_mov_b32_e32 v114, v129
	v_mov_b32_e32 v105, v129
	v_mov_b32_e32 v104, v129
	v_mov_b32_e32 v103, v129
	v_mov_b32_e32 v102, v129
	v_mov_b32_e32 v101, v129
	v_mov_b32_e32 v100, v129
	v_mov_b32_e32 v99, v129
	v_mov_b32_e32 v98, v129
	v_mov_b32_e32 v89, v129
	v_mov_b32_e32 v88, v129
	v_mov_b32_e32 v87, v129
	v_mov_b32_e32 v86, v129
	v_mov_b32_e32 v85, v129
	v_mov_b32_e32 v84, v129
	v_mov_b32_e32 v83, v129
	v_mov_b32_e32 v82, v129
	v_mov_b32_e32 v73, v129
	v_mov_b32_e32 v72, v129
	v_mov_b32_e32 v71, v129
	v_mov_b32_e32 v70, v129
	v_mov_b32_e32 v69, v129
	v_mov_b32_e32 v68, v129
	v_mov_b32_e32 v67, v129
	v_mov_b32_e32 v66, v129
	v_mov_b32_e32 v65, v129
	v_mov_b32_e32 v64, v129
	v_mov_b32_e32 v63, v129
	v_mov_b32_e32 v62, v129
	v_mov_b32_e32 v61, v129
	v_mov_b32_e32 v60, v129
	v_mov_b32_e32 v59, v129
	v_mov_b32_e32 v58, v129
	v_mov_b32_e32 v49, v129
	v_mov_b32_e32 v48, v129
	v_mov_b32_e32 v47, v129
	v_mov_b32_e32 v46, v129
	v_mov_b32_e32 v45, v129
	v_mov_b32_e32 v44, v129
	v_mov_b32_e32 v43, v129
	v_mov_b32_e32 v42, v129
	v_mov_b32_e32 v33, v129
	v_mov_b32_e32 v32, v129
	v_mov_b32_e32 v31, v129
	v_mov_b32_e32 v30, v129
	v_mov_b32_e32 v29, v129
	v_mov_b32_e32 v28, v129
	v_mov_b32_e32 v27, v129
	v_mov_b32_e32 v26, v129
	v_mov_b32_e32 v17, v129
	v_mov_b32_e32 v16, v129
	v_mov_b32_e32 v15, v129
	v_mov_b32_e32 v14, v129
	v_mov_b32_e32 v13, v129
	v_mov_b32_e32 v12, v129
	v_mov_b32_e32 v11, v129
	v_mov_b32_e32 v10, v129
	v_mov_b32_e32 v57, v129
	v_mov_b32_e32 v56, v129
	v_mov_b32_e32 v55, v129
	v_mov_b32_e32 v54, v129
	v_mov_b32_e32 v53, v129
	v_mov_b32_e32 v52, v129
	v_mov_b32_e32 v51, v129
	v_mov_b32_e32 v50, v129
	v_mov_b32_e32 v41, v129
	v_mov_b32_e32 v40, v129
	v_mov_b32_e32 v39, v129
	v_mov_b32_e32 v38, v129
	v_mov_b32_e32 v37, v129
	v_mov_b32_e32 v36, v129
	v_mov_b32_e32 v35, v129
	v_mov_b32_e32 v34, v129
	v_mov_b32_e32 v25, v129
	v_mov_b32_e32 v24, v129
	v_mov_b32_e32 v23, v129
	v_mov_b32_e32 v22, v129
	v_mov_b32_e32 v21, v129
	v_mov_b32_e32 v20, v129
	v_mov_b32_e32 v19, v129
	v_mov_b32_e32 v18, v129
	v_mov_b32_e32 v9, v129
	v_mov_b32_e32 v8, v129
	v_mov_b32_e32 v7, v129
	v_mov_b32_e32 v6, v129
	v_mov_b32_e32 v5, v129
	v_mov_b32_e32 v4, v129
	v_mov_b32_e32 v3, v129
	v_mov_b32_e32 v2, v129
	s_and_b64 vcc, exec, s[14:15]
	s_cbranch_vccnz .LBB0_1768
	s_branch .LBB0_1769
.LBB0_1845:
	s_waitcnt vmcnt(0)
	v_readlane_b32 s68, v252, 7
	v_readlane_b32 s70, v252, 9
	v_readlane_b32 s71, v252, 10
	v_readlane_b32 s76, v254, 53
	s_mov_b64 s[20:21], 0x2000
	s_barrier
	v_readlane_b32 s69, v252, 8
